# attention tile loop: MFMA burst works on fragments read in the previous interval, fragment registers refilled behind their consuming MFMA, DMA issued after the first MFMA
# speedup vs baseline: 1.0573x; 1.0156x over previous
.Lfc0_entry:
	s_lshl_b32 s0, s12, 12
	s_add_i32 s0, s91, s0
	s_lshl_b32 s1, s13, 13
	s_add_i32 s1, s91, s1
	v_add_u32_e32 v232, s0, v222
	v_add_u32_e32 v233, s0, v221
	v_add_u32_e32 v234, s1, v222
	v_add_u32_e32 v235, s1, v221
	s_add_i32 s10, s12, 3
	s_and_b32 s10, s10, 3
	s_add_i32 s33, s10, 3
	s_and_b32 s33, s33, 3
	s_lshl_b32 s33, s33, 13
	s_add_i32 s33, s33, s79
	s_addk_i32 s33, 0x4000
	s_add_i32 s32, s86, s2
	s_add_i32 s50, s32, -1
	s_mov_b32 s51, 0
	s_lshl_b64 s[50:51], s[50:51], 6
	s_add_u32 s50, s97, s50
	s_addc_u32 s51, s87, s51
	s_lshl_b32 s11, s10, 12
	s_add_i32 s11, s11, s79
	s_add_i32 s10, s32, -3
	s_cmp_lt_u32 s10, 61
	s_cselect_b32 s10, s90, s17
	s_add_i32 s48, s10, s3
	s_ashr_i32 s49, s48, 31
	s_lshl_b64 s[48:49], s[48:49], 10
	s_add_u32 s48, s95, s48
	s_addc_u32 s49, s96, s49
	s_mov_b32 m0, s11
	s_nop 0
	global_load_lds_dwordx4 v209, s[48:49]
	s_mov_b32 m0, s33
	s_nop 0
	global_load_lds_dwordx4 v218, s[50:51]
	ds_read_b128 v[144:147], v232
	ds_read_b128 v[148:151], v233
	ds_read_b128 v[152:155], v232 offset:2048
	ds_read_b128 v[156:159], v233 offset:2048
	ds_read_b128 v[176:179], v234 offset:16384
	ds_read_b128 v[180:183], v235 offset:16384
	ds_read_b128 v[168:171], v234 offset:18432
	ds_read_b128 v[172:175], v235 offset:18432
	ds_read_b128 v[192:195], v234 offset:20480
	ds_read_b128 v[196:199], v235 offset:20480
	ds_read_b128 v[184:187], v234 offset:22528
	ds_read_b128 v[188:191], v235 offset:22528
	s_add_i32 s0, s12, 1
	s_and_b32 s0, s0, 3
	s_lshl_b32 s0, s0, 12
	s_add_i32 s0, s91, s0
	s_lshl_b32 s1, s12, 13
	s_add_i32 s1, s91, s1
	v_add_u32_e32 v232, s0, v222
	v_add_u32_e32 v233, s0, v221
	v_add_u32_e32 v234, s1, v222
	v_add_u32_e32 v235, s1, v221
	s_add_i32 s10, s12, 4
	s_and_b32 s10, s10, 3
	s_add_i32 s33, s10, 3
	s_and_b32 s33, s33, 3
	s_lshl_b32 s33, s33, 13
	s_add_i32 s33, s33, s79
	s_addk_i32 s33, 0x4000
	s_add_i32 s32, s86, s2
	s_add_i32 s32, s32, 1
	s_add_i32 s50, s32, -1
	s_mov_b32 s51, 0
	s_lshl_b64 s[50:51], s[50:51], 6
	s_add_u32 s50, s97, s50
	s_addc_u32 s51, s87, s51
	s_lshl_b32 s11, s10, 12
	s_add_i32 s11, s11, s79
	s_add_i32 s10, s32, -3
	s_cmp_lt_u32 s10, 61
	s_cselect_b32 s10, s90, s17
	s_add_i32 s48, s10, s3
	s_add_i32 s48, s48, 64
	s_ashr_i32 s49, s48, 31
	s_lshl_b64 s[48:49], s[48:49], 10
	s_add_u32 s48, s95, s48
	s_addc_u32 s49, s96, s49
	s_waitcnt vmcnt(4)
	s_waitcnt lgkmcnt(0)
	s_barrier
	s_mov_b32 s13, s12
	s_add_i32 s12, s12, 1
	s_and_b32 s12, s12, 3
	s_add_i32 s2, s2, 1
	s_add_i32 s3, s3, 64
	s_cmp_lt_u32 s2, s16
	s_cbranch_scc0 .Lfc0_drainA
.Lfc0_even:
	v_mfma_scale_f32_32x32x64_f8f6f4 v[96:111], v[144:151], v[128:135], v[80:95], v220, v220 op_sel_hi:[0,0,0]
	s_mov_b32 m0, s11
	s_nop 0
	global_load_lds_dwordx4 v209, s[48:49]
	s_mov_b32 m0, s33
	s_nop 0
	global_load_lds_dwordx4 v218, s[50:51]
	s_add_i32 s10, s12, 4
	s_and_b32 s10, s10, 3
	s_add_i32 s33, s10, 3
	s_and_b32 s33, s33, 3
	s_lshl_b32 s33, s33, 13
	s_add_i32 s33, s33, s79
	s_addk_i32 s33, 0x4000
	s_add_i32 s32, s86, s2
	s_add_i32 s32, s32, 1
	s_add_i32 s50, s32, -1
	s_mov_b32 s51, 0
	s_lshl_b64 s[50:51], s[50:51], 6
	v_mfma_scale_f32_32x32x64_f8f6f4 v[112:127], v[152:159], v[128:135], v[80:95], v220, v220 op_sel_hi:[0,0,0]
	s_add_u32 s50, s97, s50
	s_addc_u32 s51, s87, s51
	s_lshl_b32 s11, s10, 12
	s_add_i32 s11, s11, s79
	s_add_i32 s10, s32, -3
	s_cmp_lt_u32 s10, 61
	s_cselect_b32 s10, s90, s17
	s_add_i32 s48, s10, s3
	s_add_i32 s48, s48, 64
	s_ashr_i32 s49, s48, 31
	s_lshl_b64 s[48:49], s[48:49], 10
	s_add_u32 s48, s95, s48
	s_addc_u32 s49, s96, s49
	v_mfma_scale_f32_32x32x64_f8f6f4 v[0:15], v[160:167], v[136:143], v[0:15], v219, v219 op_sel_hi:[0,0,0]
	ds_read_b128 v[144:147], v232
	ds_read_b128 v[148:151], v233
	ds_read_b128 v[152:155], v232 offset:2048
	ds_read_b128 v[156:159], v233 offset:2048
	v_max3_f32 v226, v96, v97, v98
	v_max3_f32 v202, v99, v100, v101
	v_max3_f32 v203, v102, v103, v104
	v_max3_f32 v211, v105, v106, v107
	v_max3_f32 v226, v226, v108, v109
	v_max3_f32 v202, v202, v110, v111
	v_max3_f32 v226, v226, v203, v211
	v_max_f32_e32 v226, v226, v202
	v_mfma_scale_f32_32x32x64_f8f6f4 v[64:79], v[160:167], v[176:183], v[64:79], v219, v219 op_sel_hi:[0,0,0]
	v_max3_f32 v227, v112, v113, v114
	v_max3_f32 v202, v115, v116, v117
	v_max3_f32 v203, v118, v119, v120
	v_max3_f32 v211, v121, v122, v123
	v_max3_f32 v227, v227, v124, v125
	v_max3_f32 v202, v202, v126, v127
	v_max3_f32 v227, v227, v203, v211
	v_max_f32_e32 v227, v227, v202
	v_max_f32_e32 v226, v226, v227
	v_mov_b32_e32 v227, v226
	s_nop 1
	v_permlane32_swap_b32_e32 v226, v227
	v_max3_f32 v226, v226, v227, v227
	s_nop 0
	v_cmp_lt_f32_e32 vcc, 0x41000000, v226
	s_cbranch_vccnz .Lfc0e_rare
	v_mfma_scale_f32_32x32x64_f8f6f4 v[48:63], v[160:167], v[168:175], v[48:63], v219, v219 op_sel_hi:[0,0,0]
	ds_read_b128 v[176:179], v234 offset:16384
	ds_read_b128 v[180:183], v235 offset:16384
	v_exp_f32_e32 v96, v96
	v_exp_f32_e32 v112, v112
	v_exp_f32_e32 v97, v97
	v_exp_f32_e32 v113, v113
	v_exp_f32_e32 v100, v100
	v_exp_f32_e32 v116, v116
	v_exp_f32_e32 v101, v101
	v_exp_f32_e32 v117, v117
	v_mfma_scale_f32_32x32x64_f8f6f4 v[32:47], v[160:167], v[192:199], v[32:47], v219, v219 op_sel_hi:[0,0,0]
	ds_read_b128 v[168:171], v234 offset:18432
	ds_read_b128 v[172:175], v235 offset:18432
	v_exp_f32_e32 v104, v104
	v_exp_f32_e32 v120, v120
	v_exp_f32_e32 v105, v105
	v_exp_f32_e32 v121, v121
	v_exp_f32_e32 v108, v108
	v_exp_f32_e32 v124, v124
	v_exp_f32_e32 v109, v109
	v_exp_f32_e32 v125, v125
	v_mfma_scale_f32_32x32x64_f8f6f4 v[16:31], v[160:167], v[184:191], v[16:31], v219, v219 op_sel_hi:[0,0,0]
	ds_read_b128 v[192:195], v234 offset:20480
	ds_read_b128 v[196:199], v235 offset:20480
	v_exp_f32_e32 v98, v98
	v_exp_f32_e32 v114, v114
	v_exp_f32_e32 v99, v99
	v_exp_f32_e32 v115, v115
	v_exp_f32_e32 v102, v102
	v_exp_f32_e32 v118, v118
	v_exp_f32_e32 v103, v103
	v_exp_f32_e32 v119, v119
	ds_read_b128 v[184:187], v234 offset:22528
	ds_read_b128 v[188:191], v235 offset:22528
.Lfc0e_join:
	v_exp_f32_e32 v106, v106
	v_exp_f32_e32 v122, v122
	v_exp_f32_e32 v107, v107
	v_exp_f32_e32 v123, v123
	v_exp_f32_e32 v110, v110
	v_exp_f32_e32 v126, v126
	v_exp_f32_e32 v111, v111
	v_exp_f32_e32 v127, v127
	s_add_i32 s0, s12, 1
	s_and_b32 s0, s0, 3
	s_lshl_b32 s0, s0, 12
	s_add_i32 s0, s91, s0
	s_lshl_b32 s1, s12, 13
	s_add_i32 s1, s91, s1
	v_add_u32_e32 v232, s0, v222
	v_add_u32_e32 v233, s0, v221
	v_add_u32_e32 v234, s1, v222
	v_add_u32_e32 v235, s1, v221
	v_cvt_pk_fp8_f32 v236, v96, v97
	v_cvt_pk_fp8_f32 v240, v112, v113
	v_cvt_pk_fp8_f32 v237, v100, v101
	v_cvt_pk_fp8_f32 v241, v116, v117
	v_cvt_pk_fp8_f32 v238, v104, v105
	v_cvt_pk_fp8_f32 v242, v120, v121
	v_cvt_pk_fp8_f32 v239, v108, v109
	v_cvt_pk_fp8_f32 v243, v124, v125
	v_cvt_pk_fp8_f32 v236, v98, v99 op_sel:[0,0,1]
	v_cvt_pk_fp8_f32 v240, v114, v115 op_sel:[0,0,1]
	v_cvt_pk_fp8_f32 v237, v102, v103 op_sel:[0,0,1]
	v_cvt_pk_fp8_f32 v241, v118, v119 op_sel:[0,0,1]
	v_cvt_pk_fp8_f32 v238, v106, v107 op_sel:[0,0,1]
	v_cvt_pk_fp8_f32 v242, v122, v123 op_sel:[0,0,1]
	v_cvt_pk_fp8_f32 v239, v110, v111 op_sel:[0,0,1]
	v_cvt_pk_fp8_f32 v243, v126, v127 op_sel:[0,0,1]
	s_waitcnt vmcnt(4)
	s_waitcnt lgkmcnt(0)
	s_barrier
	s_mov_b32 s13, s12
	s_add_i32 s12, s12, 1
	s_and_b32 s12, s12, 3
	s_add_i32 s2, s2, 1
	s_add_i32 s3, s3, 64
	s_cmp_lt_u32 s2, s16
	s_cbranch_scc1 .Lfc0_odd
	s_branch .Lfc0_drainB
.Lfc0_odd:
	v_mfma_scale_f32_32x32x64_f8f6f4 v[96:111], v[144:151], v[128:135], v[80:95], v220, v220 op_sel_hi:[0,0,0]
	s_mov_b32 m0, s11
	s_nop 0
	global_load_lds_dwordx4 v209, s[48:49]
	s_mov_b32 m0, s33
	s_nop 0
	global_load_lds_dwordx4 v218, s[50:51]
	s_add_i32 s10, s12, 4
	s_and_b32 s10, s10, 3
	s_add_i32 s33, s10, 3
	s_and_b32 s33, s33, 3
	s_lshl_b32 s33, s33, 13
	s_add_i32 s33, s33, s79
	s_addk_i32 s33, 0x4000
	s_add_i32 s32, s86, s2
	s_add_i32 s32, s32, 1
	s_add_i32 s50, s32, -1
	s_mov_b32 s51, 0
	s_lshl_b64 s[50:51], s[50:51], 6
	v_mfma_scale_f32_32x32x64_f8f6f4 v[112:127], v[152:159], v[128:135], v[80:95], v220, v220 op_sel_hi:[0,0,0]
	s_add_u32 s50, s97, s50
	s_addc_u32 s51, s87, s51
	s_lshl_b32 s11, s10, 12
	s_add_i32 s11, s11, s79
	s_add_i32 s10, s32, -3
	s_cmp_lt_u32 s10, 61
	s_cselect_b32 s10, s90, s17
	s_add_i32 s48, s10, s3
	s_add_i32 s48, s48, 64
	s_ashr_i32 s49, s48, 31
	s_lshl_b64 s[48:49], s[48:49], 10
	s_add_u32 s48, s95, s48
	s_addc_u32 s49, s96, s49
	v_mfma_scale_f32_32x32x64_f8f6f4 v[0:15], v[236:243], v[136:143], v[0:15], v219, v219 op_sel_hi:[0,0,0]
	ds_read_b128 v[144:147], v232
	ds_read_b128 v[148:151], v233
	ds_read_b128 v[152:155], v232 offset:2048
	ds_read_b128 v[156:159], v233 offset:2048
	v_max3_f32 v226, v96, v97, v98
	v_max3_f32 v202, v99, v100, v101
	v_max3_f32 v203, v102, v103, v104
	v_max3_f32 v211, v105, v106, v107
	v_max3_f32 v226, v226, v108, v109
	v_max3_f32 v202, v202, v110, v111
	v_max3_f32 v226, v226, v203, v211
	v_max_f32_e32 v226, v226, v202
	v_mfma_scale_f32_32x32x64_f8f6f4 v[64:79], v[236:243], v[176:183], v[64:79], v219, v219 op_sel_hi:[0,0,0]
	v_max3_f32 v227, v112, v113, v114
	v_max3_f32 v202, v115, v116, v117
	v_max3_f32 v203, v118, v119, v120
	v_max3_f32 v211, v121, v122, v123
	v_max3_f32 v227, v227, v124, v125
	v_max3_f32 v202, v202, v126, v127
	v_max3_f32 v227, v227, v203, v211
	v_max_f32_e32 v227, v227, v202
	v_max_f32_e32 v226, v226, v227
	v_mov_b32_e32 v227, v226
	s_nop 1
	v_permlane32_swap_b32_e32 v226, v227
	v_max3_f32 v226, v226, v227, v227
	s_nop 0
	v_cmp_lt_f32_e32 vcc, 0x41000000, v226
	s_cbranch_vccnz .Lfc0o_rare
	v_mfma_scale_f32_32x32x64_f8f6f4 v[48:63], v[236:243], v[168:175], v[48:63], v219, v219 op_sel_hi:[0,0,0]
	ds_read_b128 v[176:179], v234 offset:16384
	ds_read_b128 v[180:183], v235 offset:16384
	v_exp_f32_e32 v96, v96
	v_exp_f32_e32 v112, v112
	v_exp_f32_e32 v97, v97
	v_exp_f32_e32 v113, v113
	v_exp_f32_e32 v100, v100
	v_exp_f32_e32 v116, v116
	v_exp_f32_e32 v101, v101
	v_exp_f32_e32 v117, v117
	v_mfma_scale_f32_32x32x64_f8f6f4 v[32:47], v[236:243], v[192:199], v[32:47], v219, v219 op_sel_hi:[0,0,0]
	ds_read_b128 v[168:171], v234 offset:18432
	ds_read_b128 v[172:175], v235 offset:18432
	v_exp_f32_e32 v104, v104
	v_exp_f32_e32 v120, v120
	v_exp_f32_e32 v105, v105
	v_exp_f32_e32 v121, v121
	v_exp_f32_e32 v108, v108
	v_exp_f32_e32 v124, v124
	v_exp_f32_e32 v109, v109
	v_exp_f32_e32 v125, v125
	v_mfma_scale_f32_32x32x64_f8f6f4 v[16:31], v[236:243], v[184:191], v[16:31], v219, v219 op_sel_hi:[0,0,0]
	ds_read_b128 v[192:195], v234 offset:20480
	ds_read_b128 v[196:199], v235 offset:20480
	v_exp_f32_e32 v98, v98
	v_exp_f32_e32 v114, v114
	v_exp_f32_e32 v99, v99
	v_exp_f32_e32 v115, v115
	v_exp_f32_e32 v102, v102
	v_exp_f32_e32 v118, v118
	v_exp_f32_e32 v103, v103
	v_exp_f32_e32 v119, v119
	ds_read_b128 v[184:187], v234 offset:22528
	ds_read_b128 v[188:191], v235 offset:22528
.Lfc0o_join:
	v_exp_f32_e32 v106, v106
	v_exp_f32_e32 v122, v122
	v_exp_f32_e32 v107, v107
	v_exp_f32_e32 v123, v123
	v_exp_f32_e32 v110, v110
	v_exp_f32_e32 v126, v126
	v_exp_f32_e32 v111, v111
	v_exp_f32_e32 v127, v127
	s_add_i32 s0, s12, 1
	s_and_b32 s0, s0, 3
	s_lshl_b32 s0, s0, 12
	s_add_i32 s0, s91, s0
	s_lshl_b32 s1, s12, 13
	s_add_i32 s1, s91, s1
	v_add_u32_e32 v232, s0, v222
	v_add_u32_e32 v233, s0, v221
	v_add_u32_e32 v234, s1, v222
	v_add_u32_e32 v235, s1, v221
	v_cvt_pk_fp8_f32 v160, v96, v97
	v_cvt_pk_fp8_f32 v164, v112, v113
	v_cvt_pk_fp8_f32 v161, v100, v101
	v_cvt_pk_fp8_f32 v165, v116, v117
	v_cvt_pk_fp8_f32 v162, v104, v105
	v_cvt_pk_fp8_f32 v166, v120, v121
	v_cvt_pk_fp8_f32 v163, v108, v109
	v_cvt_pk_fp8_f32 v167, v124, v125
	v_cvt_pk_fp8_f32 v160, v98, v99 op_sel:[0,0,1]
	v_cvt_pk_fp8_f32 v164, v114, v115 op_sel:[0,0,1]
	v_cvt_pk_fp8_f32 v161, v102, v103 op_sel:[0,0,1]
	v_cvt_pk_fp8_f32 v165, v118, v119 op_sel:[0,0,1]
	v_cvt_pk_fp8_f32 v162, v106, v107 op_sel:[0,0,1]
	v_cvt_pk_fp8_f32 v166, v122, v123 op_sel:[0,0,1]
	v_cvt_pk_fp8_f32 v163, v110, v111 op_sel:[0,0,1]
	v_cvt_pk_fp8_f32 v167, v126, v127 op_sel:[0,0,1]
	s_waitcnt vmcnt(4)
	s_waitcnt lgkmcnt(0)
	s_barrier
	s_mov_b32 s13, s12
	s_add_i32 s12, s12, 1
	s_and_b32 s12, s12, 3
	s_add_i32 s2, s2, 1
	s_add_i32 s3, s3, 64
	s_cmp_lt_u32 s2, s16
	s_cbranch_scc1 .Lfc0_even
	s_branch .Lfc0_drainA
.Lfc0_drainA:
	v_mfma_scale_f32_32x32x64_f8f6f4 v[96:111], v[144:151], v[128:135], v[80:95], v220, v220 op_sel_hi:[0,0,0]
	v_mfma_scale_f32_32x32x64_f8f6f4 v[112:127], v[152:159], v[128:135], v[80:95], v220, v220 op_sel_hi:[0,0,0]
	v_mfma_scale_f32_32x32x64_f8f6f4 v[0:15], v[160:167], v[136:143], v[0:15], v219, v219 op_sel_hi:[0,0,0]
	v_max3_f32 v226, v96, v97, v98
	v_max3_f32 v202, v99, v100, v101
	v_max3_f32 v203, v102, v103, v104
	v_max3_f32 v211, v105, v106, v107
	v_max3_f32 v226, v226, v108, v109
	v_max3_f32 v202, v202, v110, v111
	v_max3_f32 v226, v226, v203, v211
	v_max_f32_e32 v226, v226, v202
	v_mfma_scale_f32_32x32x64_f8f6f4 v[64:79], v[160:167], v[176:183], v[64:79], v219, v219 op_sel_hi:[0,0,0]
	v_max3_f32 v227, v112, v113, v114
	v_max3_f32 v202, v115, v116, v117
	v_max3_f32 v203, v118, v119, v120
	v_max3_f32 v211, v121, v122, v123
	v_max3_f32 v227, v227, v124, v125
	v_max3_f32 v202, v202, v126, v127
	v_max3_f32 v227, v227, v203, v211
	v_max_f32_e32 v227, v227, v202
	v_max_f32_e32 v226, v226, v227
	v_mov_b32_e32 v227, v226
	s_nop 1
	v_permlane32_swap_b32_e32 v226, v227
	v_max3_f32 v226, v226, v227, v227
	s_nop 0
	v_cmp_lt_f32_e32 vcc, 0x41000000, v226
	s_cbranch_vccnz .Lfc0dA_rare
	v_mfma_scale_f32_32x32x64_f8f6f4 v[48:63], v[160:167], v[168:175], v[48:63], v219, v219 op_sel_hi:[0,0,0]
	v_exp_f32_e32 v96, v96
	v_exp_f32_e32 v112, v112
	v_exp_f32_e32 v97, v97
	v_exp_f32_e32 v113, v113
	v_exp_f32_e32 v100, v100
	v_exp_f32_e32 v116, v116
	v_exp_f32_e32 v101, v101
	v_exp_f32_e32 v117, v117
	v_mfma_scale_f32_32x32x64_f8f6f4 v[32:47], v[160:167], v[192:199], v[32:47], v219, v219 op_sel_hi:[0,0,0]
	v_exp_f32_e32 v104, v104
	v_exp_f32_e32 v120, v120
	v_exp_f32_e32 v105, v105
	v_exp_f32_e32 v121, v121
	v_exp_f32_e32 v108, v108
	v_exp_f32_e32 v124, v124
	v_exp_f32_e32 v109, v109
	v_exp_f32_e32 v125, v125
	v_mfma_scale_f32_32x32x64_f8f6f4 v[16:31], v[160:167], v[184:191], v[16:31], v219, v219 op_sel_hi:[0,0,0]
	v_exp_f32_e32 v98, v98
	v_exp_f32_e32 v114, v114
	v_exp_f32_e32 v99, v99
	v_exp_f32_e32 v115, v115
	v_exp_f32_e32 v102, v102
	v_exp_f32_e32 v118, v118
	v_exp_f32_e32 v103, v103
	v_exp_f32_e32 v119, v119
.Lfc0dA_join:
	v_exp_f32_e32 v106, v106
	v_exp_f32_e32 v122, v122
	v_exp_f32_e32 v107, v107
	v_exp_f32_e32 v123, v123
	v_exp_f32_e32 v110, v110
	v_exp_f32_e32 v126, v126
	v_exp_f32_e32 v111, v111
	v_exp_f32_e32 v127, v127
	v_cvt_pk_fp8_f32 v236, v96, v97
	v_cvt_pk_fp8_f32 v240, v112, v113
	v_cvt_pk_fp8_f32 v237, v100, v101
	v_cvt_pk_fp8_f32 v241, v116, v117
	v_cvt_pk_fp8_f32 v238, v104, v105
	v_cvt_pk_fp8_f32 v242, v120, v121
	v_cvt_pk_fp8_f32 v239, v108, v109
	v_cvt_pk_fp8_f32 v243, v124, v125
	v_cvt_pk_fp8_f32 v236, v98, v99 op_sel:[0,0,1]
	v_cvt_pk_fp8_f32 v240, v114, v115 op_sel:[0,0,1]
	v_cvt_pk_fp8_f32 v237, v102, v103 op_sel:[0,0,1]
	v_cvt_pk_fp8_f32 v241, v118, v119 op_sel:[0,0,1]
	v_cvt_pk_fp8_f32 v238, v106, v107 op_sel:[0,0,1]
	v_cvt_pk_fp8_f32 v242, v122, v123 op_sel:[0,0,1]
	v_cvt_pk_fp8_f32 v239, v110, v111 op_sel:[0,0,1]
	v_cvt_pk_fp8_f32 v243, v126, v127 op_sel:[0,0,1]
	s_nop 15
	s_nop 15
	s_nop 15
	s_nop 15
	v_mov_b32_e32 v160, v236
	v_mov_b32_e32 v161, v237
	v_mov_b32_e32 v162, v238
	v_mov_b32_e32 v163, v239
	v_mov_b32_e32 v164, v240
	v_mov_b32_e32 v165, v241
	v_mov_b32_e32 v166, v242
	v_mov_b32_e32 v167, v243
	s_branch .LBB0_528
.Lfc0_drainB:
	v_mfma_scale_f32_32x32x64_f8f6f4 v[96:111], v[144:151], v[128:135], v[80:95], v220, v220 op_sel_hi:[0,0,0]
	v_mfma_scale_f32_32x32x64_f8f6f4 v[112:127], v[152:159], v[128:135], v[80:95], v220, v220 op_sel_hi:[0,0,0]
	v_mfma_scale_f32_32x32x64_f8f6f4 v[0:15], v[236:243], v[136:143], v[0:15], v219, v219 op_sel_hi:[0,0,0]
	v_max3_f32 v226, v96, v97, v98
	v_max3_f32 v202, v99, v100, v101
	v_max3_f32 v203, v102, v103, v104
	v_max3_f32 v211, v105, v106, v107
	v_max3_f32 v226, v226, v108, v109
	v_max3_f32 v202, v202, v110, v111
	v_max3_f32 v226, v226, v203, v211
	v_max_f32_e32 v226, v226, v202
	v_mfma_scale_f32_32x32x64_f8f6f4 v[64:79], v[236:243], v[176:183], v[64:79], v219, v219 op_sel_hi:[0,0,0]
	v_max3_f32 v227, v112, v113, v114
	v_max3_f32 v202, v115, v116, v117
	v_max3_f32 v203, v118, v119, v120
	v_max3_f32 v211, v121, v122, v123
	v_max3_f32 v227, v227, v124, v125
	v_max3_f32 v202, v202, v126, v127
	v_max3_f32 v227, v227, v203, v211
	v_max_f32_e32 v227, v227, v202
	v_max_f32_e32 v226, v226, v227
	v_mov_b32_e32 v227, v226
	s_nop 1
	v_permlane32_swap_b32_e32 v226, v227
	v_max3_f32 v226, v226, v227, v227
	s_nop 0
	v_cmp_lt_f32_e32 vcc, 0x41000000, v226
	s_cbranch_vccnz .Lfc0dB_rare
	v_mfma_scale_f32_32x32x64_f8f6f4 v[48:63], v[236:243], v[168:175], v[48:63], v219, v219 op_sel_hi:[0,0,0]
	v_exp_f32_e32 v96, v96
	v_exp_f32_e32 v112, v112
	v_exp_f32_e32 v97, v97
	v_exp_f32_e32 v113, v113
	v_exp_f32_e32 v100, v100
	v_exp_f32_e32 v116, v116
	v_exp_f32_e32 v101, v101
	v_exp_f32_e32 v117, v117
	v_mfma_scale_f32_32x32x64_f8f6f4 v[32:47], v[236:243], v[192:199], v[32:47], v219, v219 op_sel_hi:[0,0,0]
	v_exp_f32_e32 v104, v104
	v_exp_f32_e32 v120, v120
	v_exp_f32_e32 v105, v105
	v_exp_f32_e32 v121, v121
	v_exp_f32_e32 v108, v108
	v_exp_f32_e32 v124, v124
	v_exp_f32_e32 v109, v109
	v_exp_f32_e32 v125, v125
	v_mfma_scale_f32_32x32x64_f8f6f4 v[16:31], v[236:243], v[184:191], v[16:31], v219, v219 op_sel_hi:[0,0,0]
	v_exp_f32_e32 v98, v98
	v_exp_f32_e32 v114, v114
	v_exp_f32_e32 v99, v99
	v_exp_f32_e32 v115, v115
	v_exp_f32_e32 v102, v102
	v_exp_f32_e32 v118, v118
	v_exp_f32_e32 v103, v103
	v_exp_f32_e32 v119, v119
.Lfc0dB_join:
	v_exp_f32_e32 v106, v106
	v_exp_f32_e32 v122, v122
	v_exp_f32_e32 v107, v107
	v_exp_f32_e32 v123, v123
	v_exp_f32_e32 v110, v110
	v_exp_f32_e32 v126, v126
	v_exp_f32_e32 v111, v111
	v_exp_f32_e32 v127, v127
	v_cvt_pk_fp8_f32 v160, v96, v97
	v_cvt_pk_fp8_f32 v164, v112, v113
	v_cvt_pk_fp8_f32 v161, v100, v101
	v_cvt_pk_fp8_f32 v165, v116, v117
	v_cvt_pk_fp8_f32 v162, v104, v105
	v_cvt_pk_fp8_f32 v166, v120, v121
	v_cvt_pk_fp8_f32 v163, v108, v109
	v_cvt_pk_fp8_f32 v167, v124, v125
	v_cvt_pk_fp8_f32 v160, v98, v99 op_sel:[0,0,1]
	v_cvt_pk_fp8_f32 v164, v114, v115 op_sel:[0,0,1]
	v_cvt_pk_fp8_f32 v161, v102, v103 op_sel:[0,0,1]
	v_cvt_pk_fp8_f32 v165, v118, v119 op_sel:[0,0,1]
	v_cvt_pk_fp8_f32 v162, v106, v107 op_sel:[0,0,1]
	v_cvt_pk_fp8_f32 v166, v122, v123 op_sel:[0,0,1]
	v_cvt_pk_fp8_f32 v163, v110, v111 op_sel:[0,0,1]
	v_cvt_pk_fp8_f32 v167, v126, v127 op_sel:[0,0,1]
	s_branch .LBB0_528
.Lfc0e_rare:
	v_mfma_scale_f32_32x32x64_f8f6f4 v[48:63], v[160:167], v[168:175], v[48:63], v219, v219 op_sel_hi:[0,0,0]
	ds_read_b128 v[176:179], v234 offset:16384
	ds_read_b128 v[180:183], v235 offset:16384
	v_mfma_scale_f32_32x32x64_f8f6f4 v[32:47], v[160:167], v[192:199], v[32:47], v219, v219 op_sel_hi:[0,0,0]
	ds_read_b128 v[168:171], v234 offset:18432
	ds_read_b128 v[172:175], v235 offset:18432
	v_mfma_scale_f32_32x32x64_f8f6f4 v[16:31], v[160:167], v[184:191], v[16:31], v219, v219 op_sel_hi:[0,0,0]
	ds_read_b128 v[192:195], v234 offset:20480
	ds_read_b128 v[196:199], v235 offset:20480
	s_nop 15
	s_nop 15
	s_nop 15
	s_nop 15
	s_nop 15
	ds_read_b128 v[184:187], v234 offset:22528
	ds_read_b128 v[188:191], v235 offset:22528
	v_max_f32_e32 v80, v226, v226
	v_max_f32_e32 v82, 0, v80
	s_and_saveexec_b64 s[0:1], s[6:7]
	v_exp_f32_e64 v80, -v82
	s_nop 0
	ds_write_b32 v223, v80 offset:49152
	s_or_b64 exec, exec, s[0:1]
	v_add_u32_e32 v210, s78, v224
	s_waitcnt lgkmcnt(0)
	v_add_u32_e32 v251, 0xc000, v210
	ds_read2_b32 v[228:229], v251 offset1:1
	v_add_u32_e32 v251, 0xc008, v210
	ds_read2_b32 v[230:231], v251 offset1:1
	v_add_u32_e32 v251, 0xc020, v210
	ds_read2_b32 v[244:245], v251 offset1:1
	v_add_u32_e32 v251, 0xc028, v210
	ds_read2_b32 v[246:247], v251 offset1:1
	v_add_u32_e32 v251, 0xc040, v210
	ds_read2_b32 v[248:249], v251 offset1:1
	v_add_u32_e32 v251, 0xc048, v210
	ds_read2_b32 v[206:207], v251 offset1:1
	v_add_u32_e32 v251, 0xc060, v210
	ds_read2_b32 v[252:253], v251 offset1:1
	v_add_u32_e32 v251, 0xc068, v210
	ds_read2_b32 v[202:203], v251 offset1:1
	v_add_f32_e32 v225, v225, v82
	v_xor_b32_e32 v80, 0x80000000, v225
	v_pk_add_f32 v[96:97], v[96:97], v[82:83] op_sel_hi:[1,0] neg_lo:[0,1] neg_hi:[0,1]
	v_pk_add_f32 v[112:113], v[112:113], v[82:83] op_sel_hi:[1,0] neg_lo:[0,1] neg_hi:[0,1]
	v_pk_add_f32 v[98:99], v[98:99], v[82:83] op_sel_hi:[1,0] neg_lo:[0,1] neg_hi:[0,1]
	v_pk_add_f32 v[114:115], v[114:115], v[82:83] op_sel_hi:[1,0] neg_lo:[0,1] neg_hi:[0,1]
	v_pk_add_f32 v[100:101], v[100:101], v[82:83] op_sel_hi:[1,0] neg_lo:[0,1] neg_hi:[0,1]
	v_pk_add_f32 v[116:117], v[116:117], v[82:83] op_sel_hi:[1,0] neg_lo:[0,1] neg_hi:[0,1]
	v_pk_add_f32 v[102:103], v[102:103], v[82:83] op_sel_hi:[1,0] neg_lo:[0,1] neg_hi:[0,1]
	v_pk_add_f32 v[118:119], v[118:119], v[82:83] op_sel_hi:[1,0] neg_lo:[0,1] neg_hi:[0,1]
	v_pk_add_f32 v[104:105], v[104:105], v[82:83] op_sel_hi:[1,0] neg_lo:[0,1] neg_hi:[0,1]
	v_pk_add_f32 v[120:121], v[120:121], v[82:83] op_sel_hi:[1,0] neg_lo:[0,1] neg_hi:[0,1]
	v_pk_add_f32 v[106:107], v[106:107], v[82:83] op_sel_hi:[1,0] neg_lo:[0,1] neg_hi:[0,1]
	v_pk_add_f32 v[122:123], v[122:123], v[82:83] op_sel_hi:[1,0] neg_lo:[0,1] neg_hi:[0,1]
	v_pk_add_f32 v[108:109], v[108:109], v[82:83] op_sel_hi:[1,0] neg_lo:[0,1] neg_hi:[0,1]
	v_pk_add_f32 v[124:125], v[124:125], v[82:83] op_sel_hi:[1,0] neg_lo:[0,1] neg_hi:[0,1]
	v_pk_add_f32 v[110:111], v[110:111], v[82:83] op_sel_hi:[1,0] neg_lo:[0,1] neg_hi:[0,1]
	v_pk_add_f32 v[126:127], v[126:127], v[82:83] op_sel_hi:[1,0] neg_lo:[0,1] neg_hi:[0,1]
	v_mov_b32_e32 v81, v80
	v_mov_b32_e32 v82, v80
	v_mov_b32_e32 v83, v80
	v_mov_b32_e32 v84, v80
	v_mov_b32_e32 v85, v80
	v_mov_b32_e32 v86, v80
	v_mov_b32_e32 v87, v80
	v_mov_b32_e32 v88, v80
	v_mov_b32_e32 v89, v80
	v_mov_b32_e32 v90, v80
	v_mov_b32_e32 v91, v80
	v_mov_b32_e32 v92, v80
	v_mov_b32_e32 v93, v80
	v_mov_b32_e32 v94, v80
	v_mov_b32_e32 v95, v80
	s_waitcnt lgkmcnt(0)
	v_pk_mul_f32 v[64:65], v[64:65], v[228:229]
	v_pk_mul_f32 v[66:67], v[66:67], v[230:231]
	v_pk_mul_f32 v[68:69], v[68:69], v[244:245]
	v_pk_mul_f32 v[70:71], v[70:71], v[246:247]
	v_pk_mul_f32 v[72:73], v[72:73], v[248:249]
	v_pk_mul_f32 v[74:75], v[74:75], v[206:207]
	v_pk_mul_f32 v[76:77], v[76:77], v[252:253]
	v_pk_mul_f32 v[78:79], v[78:79], v[202:203]
	v_pk_mul_f32 v[48:49], v[48:49], v[228:229]
	v_pk_mul_f32 v[50:51], v[50:51], v[230:231]
	v_pk_mul_f32 v[52:53], v[52:53], v[244:245]
	v_pk_mul_f32 v[54:55], v[54:55], v[246:247]
	v_pk_mul_f32 v[56:57], v[56:57], v[248:249]
	v_pk_mul_f32 v[58:59], v[58:59], v[206:207]
	v_pk_mul_f32 v[60:61], v[60:61], v[252:253]
	v_pk_mul_f32 v[62:63], v[62:63], v[202:203]
	v_pk_mul_f32 v[32:33], v[32:33], v[228:229]
	v_pk_mul_f32 v[34:35], v[34:35], v[230:231]
	v_pk_mul_f32 v[36:37], v[36:37], v[244:245]
	v_pk_mul_f32 v[38:39], v[38:39], v[246:247]
	v_pk_mul_f32 v[40:41], v[40:41], v[248:249]
	v_pk_mul_f32 v[42:43], v[42:43], v[206:207]
	v_pk_mul_f32 v[44:45], v[44:45], v[252:253]
	v_pk_mul_f32 v[46:47], v[46:47], v[202:203]
	v_pk_mul_f32 v[16:17], v[16:17], v[228:229]
	v_pk_mul_f32 v[18:19], v[18:19], v[230:231]
	v_pk_mul_f32 v[20:21], v[20:21], v[244:245]
	v_pk_mul_f32 v[22:23], v[22:23], v[246:247]
	v_pk_mul_f32 v[24:25], v[24:25], v[248:249]
	v_pk_mul_f32 v[26:27], v[26:27], v[206:207]
	v_pk_mul_f32 v[28:29], v[28:29], v[252:253]
	v_pk_mul_f32 v[30:31], v[30:31], v[202:203]
	v_pk_mul_f32 v[0:1], v[0:1], v[228:229]
	v_pk_mul_f32 v[2:3], v[2:3], v[230:231]
	v_pk_mul_f32 v[4:5], v[4:5], v[244:245]
	v_pk_mul_f32 v[6:7], v[6:7], v[246:247]
	v_pk_mul_f32 v[8:9], v[8:9], v[248:249]
	v_pk_mul_f32 v[10:11], v[10:11], v[206:207]
	v_pk_mul_f32 v[12:13], v[12:13], v[252:253]
	v_pk_mul_f32 v[14:15], v[14:15], v[202:203]
	v_exp_f32_e32 v96, v96
	v_exp_f32_e32 v112, v112
	v_exp_f32_e32 v97, v97
	v_exp_f32_e32 v113, v113
	v_exp_f32_e32 v100, v100
	v_exp_f32_e32 v116, v116
	v_exp_f32_e32 v101, v101
	v_exp_f32_e32 v117, v117
	v_exp_f32_e32 v104, v104
	v_exp_f32_e32 v120, v120
	v_exp_f32_e32 v105, v105
	v_exp_f32_e32 v121, v121
	v_exp_f32_e32 v108, v108
	v_exp_f32_e32 v124, v124
	v_exp_f32_e32 v109, v109
	v_exp_f32_e32 v125, v125
	v_exp_f32_e32 v98, v98
	v_exp_f32_e32 v114, v114
	v_exp_f32_e32 v99, v99
	v_exp_f32_e32 v115, v115
	v_exp_f32_e32 v102, v102
	v_exp_f32_e32 v118, v118
	v_exp_f32_e32 v103, v103
	v_exp_f32_e32 v119, v119
	s_branch .Lfc0e_join
.Lfc0o_rare:
	v_mfma_scale_f32_32x32x64_f8f6f4 v[48:63], v[236:243], v[168:175], v[48:63], v219, v219 op_sel_hi:[0,0,0]
	ds_read_b128 v[176:179], v234 offset:16384
	ds_read_b128 v[180:183], v235 offset:16384
	v_mfma_scale_f32_32x32x64_f8f6f4 v[32:47], v[236:243], v[192:199], v[32:47], v219, v219 op_sel_hi:[0,0,0]
	ds_read_b128 v[168:171], v234 offset:18432
	ds_read_b128 v[172:175], v235 offset:18432
	v_mfma_scale_f32_32x32x64_f8f6f4 v[16:31], v[236:243], v[184:191], v[16:31], v219, v219 op_sel_hi:[0,0,0]
	ds_read_b128 v[192:195], v234 offset:20480
	ds_read_b128 v[196:199], v235 offset:20480
	s_nop 15
	s_nop 15
	s_nop 15
	s_nop 15
	s_nop 15
	ds_read_b128 v[184:187], v234 offset:22528
	ds_read_b128 v[188:191], v235 offset:22528
	v_max_f32_e32 v80, v226, v226
	v_max_f32_e32 v82, 0, v80
	s_and_saveexec_b64 s[0:1], s[6:7]
	v_exp_f32_e64 v80, -v82
	s_nop 0
	ds_write_b32 v223, v80 offset:49152
	s_or_b64 exec, exec, s[0:1]
	v_add_u32_e32 v210, s78, v224
	s_waitcnt lgkmcnt(0)
	v_add_u32_e32 v251, 0xc000, v210
	ds_read2_b32 v[228:229], v251 offset1:1
	v_add_u32_e32 v251, 0xc008, v210
	ds_read2_b32 v[230:231], v251 offset1:1
	v_add_u32_e32 v251, 0xc020, v210
	ds_read2_b32 v[244:245], v251 offset1:1
	v_add_u32_e32 v251, 0xc028, v210
	ds_read2_b32 v[246:247], v251 offset1:1
	v_add_u32_e32 v251, 0xc040, v210
	ds_read2_b32 v[248:249], v251 offset1:1
	v_add_u32_e32 v251, 0xc048, v210
	ds_read2_b32 v[206:207], v251 offset1:1
	v_add_u32_e32 v251, 0xc060, v210
	ds_read2_b32 v[252:253], v251 offset1:1
	v_add_u32_e32 v251, 0xc068, v210
	ds_read2_b32 v[202:203], v251 offset1:1
	v_add_f32_e32 v225, v225, v82
	v_xor_b32_e32 v80, 0x80000000, v225
	v_pk_add_f32 v[96:97], v[96:97], v[82:83] op_sel_hi:[1,0] neg_lo:[0,1] neg_hi:[0,1]
	v_pk_add_f32 v[112:113], v[112:113], v[82:83] op_sel_hi:[1,0] neg_lo:[0,1] neg_hi:[0,1]
	v_pk_add_f32 v[98:99], v[98:99], v[82:83] op_sel_hi:[1,0] neg_lo:[0,1] neg_hi:[0,1]
	v_pk_add_f32 v[114:115], v[114:115], v[82:83] op_sel_hi:[1,0] neg_lo:[0,1] neg_hi:[0,1]
	v_pk_add_f32 v[100:101], v[100:101], v[82:83] op_sel_hi:[1,0] neg_lo:[0,1] neg_hi:[0,1]
	v_pk_add_f32 v[116:117], v[116:117], v[82:83] op_sel_hi:[1,0] neg_lo:[0,1] neg_hi:[0,1]
	v_pk_add_f32 v[102:103], v[102:103], v[82:83] op_sel_hi:[1,0] neg_lo:[0,1] neg_hi:[0,1]
	v_pk_add_f32 v[118:119], v[118:119], v[82:83] op_sel_hi:[1,0] neg_lo:[0,1] neg_hi:[0,1]
	v_pk_add_f32 v[104:105], v[104:105], v[82:83] op_sel_hi:[1,0] neg_lo:[0,1] neg_hi:[0,1]
	v_pk_add_f32 v[120:121], v[120:121], v[82:83] op_sel_hi:[1,0] neg_lo:[0,1] neg_hi:[0,1]
	v_pk_add_f32 v[106:107], v[106:107], v[82:83] op_sel_hi:[1,0] neg_lo:[0,1] neg_hi:[0,1]
	v_pk_add_f32 v[122:123], v[122:123], v[82:83] op_sel_hi:[1,0] neg_lo:[0,1] neg_hi:[0,1]
	v_pk_add_f32 v[108:109], v[108:109], v[82:83] op_sel_hi:[1,0] neg_lo:[0,1] neg_hi:[0,1]
	v_pk_add_f32 v[124:125], v[124:125], v[82:83] op_sel_hi:[1,0] neg_lo:[0,1] neg_hi:[0,1]
	v_pk_add_f32 v[110:111], v[110:111], v[82:83] op_sel_hi:[1,0] neg_lo:[0,1] neg_hi:[0,1]
	v_pk_add_f32 v[126:127], v[126:127], v[82:83] op_sel_hi:[1,0] neg_lo:[0,1] neg_hi:[0,1]
	v_mov_b32_e32 v81, v80
	v_mov_b32_e32 v82, v80
	v_mov_b32_e32 v83, v80
	v_mov_b32_e32 v84, v80
	v_mov_b32_e32 v85, v80
	v_mov_b32_e32 v86, v80
	v_mov_b32_e32 v87, v80
	v_mov_b32_e32 v88, v80
	v_mov_b32_e32 v89, v80
	v_mov_b32_e32 v90, v80
	v_mov_b32_e32 v91, v80
	v_mov_b32_e32 v92, v80
	v_mov_b32_e32 v93, v80
	v_mov_b32_e32 v94, v80
	v_mov_b32_e32 v95, v80
	s_waitcnt lgkmcnt(0)
	v_pk_mul_f32 v[64:65], v[64:65], v[228:229]
	v_pk_mul_f32 v[66:67], v[66:67], v[230:231]
	v_pk_mul_f32 v[68:69], v[68:69], v[244:245]
	v_pk_mul_f32 v[70:71], v[70:71], v[246:247]
	v_pk_mul_f32 v[72:73], v[72:73], v[248:249]
	v_pk_mul_f32 v[74:75], v[74:75], v[206:207]
	v_pk_mul_f32 v[76:77], v[76:77], v[252:253]
	v_pk_mul_f32 v[78:79], v[78:79], v[202:203]
	v_pk_mul_f32 v[48:49], v[48:49], v[228:229]
	v_pk_mul_f32 v[50:51], v[50:51], v[230:231]
	v_pk_mul_f32 v[52:53], v[52:53], v[244:245]
	v_pk_mul_f32 v[54:55], v[54:55], v[246:247]
	v_pk_mul_f32 v[56:57], v[56:57], v[248:249]
	v_pk_mul_f32 v[58:59], v[58:59], v[206:207]
	v_pk_mul_f32 v[60:61], v[60:61], v[252:253]
	v_pk_mul_f32 v[62:63], v[62:63], v[202:203]
	v_pk_mul_f32 v[32:33], v[32:33], v[228:229]
	v_pk_mul_f32 v[34:35], v[34:35], v[230:231]
	v_pk_mul_f32 v[36:37], v[36:37], v[244:245]
	v_pk_mul_f32 v[38:39], v[38:39], v[246:247]
	v_pk_mul_f32 v[40:41], v[40:41], v[248:249]
	v_pk_mul_f32 v[42:43], v[42:43], v[206:207]
	v_pk_mul_f32 v[44:45], v[44:45], v[252:253]
	v_pk_mul_f32 v[46:47], v[46:47], v[202:203]
	v_pk_mul_f32 v[16:17], v[16:17], v[228:229]
	v_pk_mul_f32 v[18:19], v[18:19], v[230:231]
	v_pk_mul_f32 v[20:21], v[20:21], v[244:245]
	v_pk_mul_f32 v[22:23], v[22:23], v[246:247]
	v_pk_mul_f32 v[24:25], v[24:25], v[248:249]
	v_pk_mul_f32 v[26:27], v[26:27], v[206:207]
	v_pk_mul_f32 v[28:29], v[28:29], v[252:253]
	v_pk_mul_f32 v[30:31], v[30:31], v[202:203]
	v_pk_mul_f32 v[0:1], v[0:1], v[228:229]
	v_pk_mul_f32 v[2:3], v[2:3], v[230:231]
	v_pk_mul_f32 v[4:5], v[4:5], v[244:245]
	v_pk_mul_f32 v[6:7], v[6:7], v[246:247]
	v_pk_mul_f32 v[8:9], v[8:9], v[248:249]
	v_pk_mul_f32 v[10:11], v[10:11], v[206:207]
	v_pk_mul_f32 v[12:13], v[12:13], v[252:253]
	v_pk_mul_f32 v[14:15], v[14:15], v[202:203]
	v_exp_f32_e32 v96, v96
	v_exp_f32_e32 v112, v112
	v_exp_f32_e32 v97, v97
	v_exp_f32_e32 v113, v113
	v_exp_f32_e32 v100, v100
	v_exp_f32_e32 v116, v116
	v_exp_f32_e32 v101, v101
	v_exp_f32_e32 v117, v117
	v_exp_f32_e32 v104, v104
	v_exp_f32_e32 v120, v120
	v_exp_f32_e32 v105, v105
	v_exp_f32_e32 v121, v121
	v_exp_f32_e32 v108, v108
	v_exp_f32_e32 v124, v124
	v_exp_f32_e32 v109, v109
	v_exp_f32_e32 v125, v125
	v_exp_f32_e32 v98, v98
	v_exp_f32_e32 v114, v114
	v_exp_f32_e32 v99, v99
	v_exp_f32_e32 v115, v115
	v_exp_f32_e32 v102, v102
	v_exp_f32_e32 v118, v118
	v_exp_f32_e32 v103, v103
	v_exp_f32_e32 v119, v119
	s_branch .Lfc0o_join
.Lfc0dA_rare:
	v_mfma_scale_f32_32x32x64_f8f6f4 v[48:63], v[160:167], v[168:175], v[48:63], v219, v219 op_sel_hi:[0,0,0]
	v_mfma_scale_f32_32x32x64_f8f6f4 v[32:47], v[160:167], v[192:199], v[32:47], v219, v219 op_sel_hi:[0,0,0]
	v_mfma_scale_f32_32x32x64_f8f6f4 v[16:31], v[160:167], v[184:191], v[16:31], v219, v219 op_sel_hi:[0,0,0]
	s_nop 15
	s_nop 15
	s_nop 15
	s_nop 15
	s_nop 15
	v_max_f32_e32 v80, v226, v226
	v_max_f32_e32 v82, 0, v80
	s_and_saveexec_b64 s[0:1], s[6:7]
	v_exp_f32_e64 v80, -v82
	s_nop 0
	ds_write_b32 v223, v80 offset:49152
	s_or_b64 exec, exec, s[0:1]
	v_add_u32_e32 v210, s78, v224
	s_waitcnt lgkmcnt(0)
	v_add_u32_e32 v251, 0xc000, v210
	ds_read2_b32 v[228:229], v251 offset1:1
	v_add_u32_e32 v251, 0xc008, v210
	ds_read2_b32 v[230:231], v251 offset1:1
	v_add_u32_e32 v251, 0xc020, v210
	ds_read2_b32 v[244:245], v251 offset1:1
	v_add_u32_e32 v251, 0xc028, v210
	ds_read2_b32 v[246:247], v251 offset1:1
	v_add_u32_e32 v251, 0xc040, v210
	ds_read2_b32 v[248:249], v251 offset1:1
	v_add_u32_e32 v251, 0xc048, v210
	ds_read2_b32 v[206:207], v251 offset1:1
	v_add_u32_e32 v251, 0xc060, v210
	ds_read2_b32 v[252:253], v251 offset1:1
	v_add_u32_e32 v251, 0xc068, v210
	ds_read2_b32 v[202:203], v251 offset1:1
	v_add_f32_e32 v225, v225, v82
	v_xor_b32_e32 v80, 0x80000000, v225
	v_pk_add_f32 v[96:97], v[96:97], v[82:83] op_sel_hi:[1,0] neg_lo:[0,1] neg_hi:[0,1]
	v_pk_add_f32 v[112:113], v[112:113], v[82:83] op_sel_hi:[1,0] neg_lo:[0,1] neg_hi:[0,1]
	v_pk_add_f32 v[98:99], v[98:99], v[82:83] op_sel_hi:[1,0] neg_lo:[0,1] neg_hi:[0,1]
	v_pk_add_f32 v[114:115], v[114:115], v[82:83] op_sel_hi:[1,0] neg_lo:[0,1] neg_hi:[0,1]
	v_pk_add_f32 v[100:101], v[100:101], v[82:83] op_sel_hi:[1,0] neg_lo:[0,1] neg_hi:[0,1]
	v_pk_add_f32 v[116:117], v[116:117], v[82:83] op_sel_hi:[1,0] neg_lo:[0,1] neg_hi:[0,1]
	v_pk_add_f32 v[102:103], v[102:103], v[82:83] op_sel_hi:[1,0] neg_lo:[0,1] neg_hi:[0,1]
	v_pk_add_f32 v[118:119], v[118:119], v[82:83] op_sel_hi:[1,0] neg_lo:[0,1] neg_hi:[0,1]
	v_pk_add_f32 v[104:105], v[104:105], v[82:83] op_sel_hi:[1,0] neg_lo:[0,1] neg_hi:[0,1]
	v_pk_add_f32 v[120:121], v[120:121], v[82:83] op_sel_hi:[1,0] neg_lo:[0,1] neg_hi:[0,1]
	v_pk_add_f32 v[106:107], v[106:107], v[82:83] op_sel_hi:[1,0] neg_lo:[0,1] neg_hi:[0,1]
	v_pk_add_f32 v[122:123], v[122:123], v[82:83] op_sel_hi:[1,0] neg_lo:[0,1] neg_hi:[0,1]
	v_pk_add_f32 v[108:109], v[108:109], v[82:83] op_sel_hi:[1,0] neg_lo:[0,1] neg_hi:[0,1]
	v_pk_add_f32 v[124:125], v[124:125], v[82:83] op_sel_hi:[1,0] neg_lo:[0,1] neg_hi:[0,1]
	v_pk_add_f32 v[110:111], v[110:111], v[82:83] op_sel_hi:[1,0] neg_lo:[0,1] neg_hi:[0,1]
	v_pk_add_f32 v[126:127], v[126:127], v[82:83] op_sel_hi:[1,0] neg_lo:[0,1] neg_hi:[0,1]
	v_mov_b32_e32 v81, v80
	v_mov_b32_e32 v82, v80
	v_mov_b32_e32 v83, v80
	v_mov_b32_e32 v84, v80
	v_mov_b32_e32 v85, v80
	v_mov_b32_e32 v86, v80
	v_mov_b32_e32 v87, v80
	v_mov_b32_e32 v88, v80
	v_mov_b32_e32 v89, v80
	v_mov_b32_e32 v90, v80
	v_mov_b32_e32 v91, v80
	v_mov_b32_e32 v92, v80
	v_mov_b32_e32 v93, v80
	v_mov_b32_e32 v94, v80
	v_mov_b32_e32 v95, v80
	s_waitcnt lgkmcnt(0)
	v_pk_mul_f32 v[64:65], v[64:65], v[228:229]
	v_pk_mul_f32 v[66:67], v[66:67], v[230:231]
	v_pk_mul_f32 v[68:69], v[68:69], v[244:245]
	v_pk_mul_f32 v[70:71], v[70:71], v[246:247]
	v_pk_mul_f32 v[72:73], v[72:73], v[248:249]
	v_pk_mul_f32 v[74:75], v[74:75], v[206:207]
	v_pk_mul_f32 v[76:77], v[76:77], v[252:253]
	v_pk_mul_f32 v[78:79], v[78:79], v[202:203]
	v_pk_mul_f32 v[48:49], v[48:49], v[228:229]
	v_pk_mul_f32 v[50:51], v[50:51], v[230:231]
	v_pk_mul_f32 v[52:53], v[52:53], v[244:245]
	v_pk_mul_f32 v[54:55], v[54:55], v[246:247]
	v_pk_mul_f32 v[56:57], v[56:57], v[248:249]
	v_pk_mul_f32 v[58:59], v[58:59], v[206:207]
	v_pk_mul_f32 v[60:61], v[60:61], v[252:253]
	v_pk_mul_f32 v[62:63], v[62:63], v[202:203]
	v_pk_mul_f32 v[32:33], v[32:33], v[228:229]
	v_pk_mul_f32 v[34:35], v[34:35], v[230:231]
	v_pk_mul_f32 v[36:37], v[36:37], v[244:245]
	v_pk_mul_f32 v[38:39], v[38:39], v[246:247]
	v_pk_mul_f32 v[40:41], v[40:41], v[248:249]
	v_pk_mul_f32 v[42:43], v[42:43], v[206:207]
	v_pk_mul_f32 v[44:45], v[44:45], v[252:253]
	v_pk_mul_f32 v[46:47], v[46:47], v[202:203]
	v_pk_mul_f32 v[16:17], v[16:17], v[228:229]
	v_pk_mul_f32 v[18:19], v[18:19], v[230:231]
	v_pk_mul_f32 v[20:21], v[20:21], v[244:245]
	v_pk_mul_f32 v[22:23], v[22:23], v[246:247]
	v_pk_mul_f32 v[24:25], v[24:25], v[248:249]
	v_pk_mul_f32 v[26:27], v[26:27], v[206:207]
	v_pk_mul_f32 v[28:29], v[28:29], v[252:253]
	v_pk_mul_f32 v[30:31], v[30:31], v[202:203]
	v_pk_mul_f32 v[0:1], v[0:1], v[228:229]
	v_pk_mul_f32 v[2:3], v[2:3], v[230:231]
	v_pk_mul_f32 v[4:5], v[4:5], v[244:245]
	v_pk_mul_f32 v[6:7], v[6:7], v[246:247]
	v_pk_mul_f32 v[8:9], v[8:9], v[248:249]
	v_pk_mul_f32 v[10:11], v[10:11], v[206:207]
	v_pk_mul_f32 v[12:13], v[12:13], v[252:253]
	v_pk_mul_f32 v[14:15], v[14:15], v[202:203]
	v_exp_f32_e32 v96, v96
	v_exp_f32_e32 v112, v112
	v_exp_f32_e32 v97, v97
	v_exp_f32_e32 v113, v113
	v_exp_f32_e32 v100, v100
	v_exp_f32_e32 v116, v116
	v_exp_f32_e32 v101, v101
	v_exp_f32_e32 v117, v117
	v_exp_f32_e32 v104, v104
	v_exp_f32_e32 v120, v120
	v_exp_f32_e32 v105, v105
	v_exp_f32_e32 v121, v121
	v_exp_f32_e32 v108, v108
	v_exp_f32_e32 v124, v124
	v_exp_f32_e32 v109, v109
	v_exp_f32_e32 v125, v125
	v_exp_f32_e32 v98, v98
	v_exp_f32_e32 v114, v114
	v_exp_f32_e32 v99, v99
	v_exp_f32_e32 v115, v115
	v_exp_f32_e32 v102, v102
	v_exp_f32_e32 v118, v118
	v_exp_f32_e32 v103, v103
	v_exp_f32_e32 v119, v119
	s_branch .Lfc0dA_join
.Lfc0dB_rare:
	v_mfma_scale_f32_32x32x64_f8f6f4 v[48:63], v[236:243], v[168:175], v[48:63], v219, v219 op_sel_hi:[0,0,0]
	v_mfma_scale_f32_32x32x64_f8f6f4 v[32:47], v[236:243], v[192:199], v[32:47], v219, v219 op_sel_hi:[0,0,0]
	v_mfma_scale_f32_32x32x64_f8f6f4 v[16:31], v[236:243], v[184:191], v[16:31], v219, v219 op_sel_hi:[0,0,0]
	s_nop 15
	s_nop 15
	s_nop 15
	s_nop 15
	s_nop 15
	v_max_f32_e32 v80, v226, v226
	v_max_f32_e32 v82, 0, v80
	s_and_saveexec_b64 s[0:1], s[6:7]
	v_exp_f32_e64 v80, -v82
	s_nop 0
	ds_write_b32 v223, v80 offset:49152
	s_or_b64 exec, exec, s[0:1]
	v_add_u32_e32 v210, s78, v224
	s_waitcnt lgkmcnt(0)
	v_add_u32_e32 v251, 0xc000, v210
	ds_read2_b32 v[228:229], v251 offset1:1
	v_add_u32_e32 v251, 0xc008, v210
	ds_read2_b32 v[230:231], v251 offset1:1
	v_add_u32_e32 v251, 0xc020, v210
	ds_read2_b32 v[244:245], v251 offset1:1
	v_add_u32_e32 v251, 0xc028, v210
	ds_read2_b32 v[246:247], v251 offset1:1
	v_add_u32_e32 v251, 0xc040, v210
	ds_read2_b32 v[248:249], v251 offset1:1
	v_add_u32_e32 v251, 0xc048, v210
	ds_read2_b32 v[206:207], v251 offset1:1
	v_add_u32_e32 v251, 0xc060, v210
	ds_read2_b32 v[252:253], v251 offset1:1
	v_add_u32_e32 v251, 0xc068, v210
	ds_read2_b32 v[202:203], v251 offset1:1
	v_add_f32_e32 v225, v225, v82
	v_xor_b32_e32 v80, 0x80000000, v225
	v_pk_add_f32 v[96:97], v[96:97], v[82:83] op_sel_hi:[1,0] neg_lo:[0,1] neg_hi:[0,1]
	v_pk_add_f32 v[112:113], v[112:113], v[82:83] op_sel_hi:[1,0] neg_lo:[0,1] neg_hi:[0,1]
	v_pk_add_f32 v[98:99], v[98:99], v[82:83] op_sel_hi:[1,0] neg_lo:[0,1] neg_hi:[0,1]
	v_pk_add_f32 v[114:115], v[114:115], v[82:83] op_sel_hi:[1,0] neg_lo:[0,1] neg_hi:[0,1]
	v_pk_add_f32 v[100:101], v[100:101], v[82:83] op_sel_hi:[1,0] neg_lo:[0,1] neg_hi:[0,1]
	v_pk_add_f32 v[116:117], v[116:117], v[82:83] op_sel_hi:[1,0] neg_lo:[0,1] neg_hi:[0,1]
	v_pk_add_f32 v[102:103], v[102:103], v[82:83] op_sel_hi:[1,0] neg_lo:[0,1] neg_hi:[0,1]
	v_pk_add_f32 v[118:119], v[118:119], v[82:83] op_sel_hi:[1,0] neg_lo:[0,1] neg_hi:[0,1]
	v_pk_add_f32 v[104:105], v[104:105], v[82:83] op_sel_hi:[1,0] neg_lo:[0,1] neg_hi:[0,1]
	v_pk_add_f32 v[120:121], v[120:121], v[82:83] op_sel_hi:[1,0] neg_lo:[0,1] neg_hi:[0,1]
	v_pk_add_f32 v[106:107], v[106:107], v[82:83] op_sel_hi:[1,0] neg_lo:[0,1] neg_hi:[0,1]
	v_pk_add_f32 v[122:123], v[122:123], v[82:83] op_sel_hi:[1,0] neg_lo:[0,1] neg_hi:[0,1]
	v_pk_add_f32 v[108:109], v[108:109], v[82:83] op_sel_hi:[1,0] neg_lo:[0,1] neg_hi:[0,1]
	v_pk_add_f32 v[124:125], v[124:125], v[82:83] op_sel_hi:[1,0] neg_lo:[0,1] neg_hi:[0,1]
	v_pk_add_f32 v[110:111], v[110:111], v[82:83] op_sel_hi:[1,0] neg_lo:[0,1] neg_hi:[0,1]
	v_pk_add_f32 v[126:127], v[126:127], v[82:83] op_sel_hi:[1,0] neg_lo:[0,1] neg_hi:[0,1]
	v_mov_b32_e32 v81, v80
	v_mov_b32_e32 v82, v80
	v_mov_b32_e32 v83, v80
	v_mov_b32_e32 v84, v80
	v_mov_b32_e32 v85, v80
	v_mov_b32_e32 v86, v80
	v_mov_b32_e32 v87, v80
	v_mov_b32_e32 v88, v80
	v_mov_b32_e32 v89, v80
	v_mov_b32_e32 v90, v80
	v_mov_b32_e32 v91, v80
	v_mov_b32_e32 v92, v80
	v_mov_b32_e32 v93, v80
	v_mov_b32_e32 v94, v80
	v_mov_b32_e32 v95, v80
	s_waitcnt lgkmcnt(0)
	v_pk_mul_f32 v[64:65], v[64:65], v[228:229]
	v_pk_mul_f32 v[66:67], v[66:67], v[230:231]
	v_pk_mul_f32 v[68:69], v[68:69], v[244:245]
	v_pk_mul_f32 v[70:71], v[70:71], v[246:247]
	v_pk_mul_f32 v[72:73], v[72:73], v[248:249]
	v_pk_mul_f32 v[74:75], v[74:75], v[206:207]
	v_pk_mul_f32 v[76:77], v[76:77], v[252:253]
	v_pk_mul_f32 v[78:79], v[78:79], v[202:203]
	v_pk_mul_f32 v[48:49], v[48:49], v[228:229]
	v_pk_mul_f32 v[50:51], v[50:51], v[230:231]
	v_pk_mul_f32 v[52:53], v[52:53], v[244:245]
	v_pk_mul_f32 v[54:55], v[54:55], v[246:247]
	v_pk_mul_f32 v[56:57], v[56:57], v[248:249]
	v_pk_mul_f32 v[58:59], v[58:59], v[206:207]
	v_pk_mul_f32 v[60:61], v[60:61], v[252:253]
	v_pk_mul_f32 v[62:63], v[62:63], v[202:203]
	v_pk_mul_f32 v[32:33], v[32:33], v[228:229]
	v_pk_mul_f32 v[34:35], v[34:35], v[230:231]
	v_pk_mul_f32 v[36:37], v[36:37], v[244:245]
	v_pk_mul_f32 v[38:39], v[38:39], v[246:247]
	v_pk_mul_f32 v[40:41], v[40:41], v[248:249]
	v_pk_mul_f32 v[42:43], v[42:43], v[206:207]
	v_pk_mul_f32 v[44:45], v[44:45], v[252:253]
	v_pk_mul_f32 v[46:47], v[46:47], v[202:203]
	v_pk_mul_f32 v[16:17], v[16:17], v[228:229]
	v_pk_mul_f32 v[18:19], v[18:19], v[230:231]
	v_pk_mul_f32 v[20:21], v[20:21], v[244:245]
	v_pk_mul_f32 v[22:23], v[22:23], v[246:247]
	v_pk_mul_f32 v[24:25], v[24:25], v[248:249]
	v_pk_mul_f32 v[26:27], v[26:27], v[206:207]
	v_pk_mul_f32 v[28:29], v[28:29], v[252:253]
	v_pk_mul_f32 v[30:31], v[30:31], v[202:203]
	v_pk_mul_f32 v[0:1], v[0:1], v[228:229]
	v_pk_mul_f32 v[2:3], v[2:3], v[230:231]
	v_pk_mul_f32 v[4:5], v[4:5], v[244:245]
	v_pk_mul_f32 v[6:7], v[6:7], v[246:247]
	v_pk_mul_f32 v[8:9], v[8:9], v[248:249]
	v_pk_mul_f32 v[10:11], v[10:11], v[206:207]
	v_pk_mul_f32 v[12:13], v[12:13], v[252:253]
	v_pk_mul_f32 v[14:15], v[14:15], v[202:203]
	v_exp_f32_e32 v96, v96
	v_exp_f32_e32 v112, v112
	v_exp_f32_e32 v97, v97
	v_exp_f32_e32 v113, v113
	v_exp_f32_e32 v100, v100
	v_exp_f32_e32 v116, v116
	v_exp_f32_e32 v101, v101
	v_exp_f32_e32 v117, v117
	v_exp_f32_e32 v104, v104
	v_exp_f32_e32 v120, v120
	v_exp_f32_e32 v105, v105
	v_exp_f32_e32 v121, v121
	v_exp_f32_e32 v108, v108
	v_exp_f32_e32 v124, v124
	v_exp_f32_e32 v109, v109
	v_exp_f32_e32 v125, v125
	v_exp_f32_e32 v98, v98
	v_exp_f32_e32 v114, v114
	v_exp_f32_e32 v99, v99
	v_exp_f32_e32 v115, v115
	v_exp_f32_e32 v102, v102
	v_exp_f32_e32 v118, v118
	v_exp_f32_e32 v103, v103
	v_exp_f32_e32 v119, v119
	s_branch .Lfc0dB_join
.Lfc1_entry:
	v_max3_f32 v226, v96, v97, v98
	v_max3_f32 v202, v99, v100, v101
	v_max3_f32 v203, v102, v103, v104
	v_max3_f32 v211, v105, v106, v107
	v_max3_f32 v226, v226, v108, v109
	v_max3_f32 v202, v202, v110, v111
	v_max3_f32 v226, v226, v203, v211
	v_max_f32_e32 v226, v226, v202
	v_max3_f32 v227, v112, v113, v114
	v_max3_f32 v202, v115, v116, v117
	v_max3_f32 v203, v118, v119, v120
	v_max3_f32 v211, v121, v122, v123
	v_max3_f32 v227, v227, v124, v125
	v_max3_f32 v202, v202, v126, v127
	v_max3_f32 v227, v227, v203, v211
	v_max_f32_e32 v227, v227, v202
	v_max_f32_e32 v226, v226, v227
	v_mov_b32_e32 v227, v226
	s_nop 1
	v_permlane32_swap_b32_e32 v226, v227
	v_max3_f32 v226, v226, v227, v227
	s_nop 0
	v_cmp_lt_f32_e32 vcc, 0x41000000, v226
	s_cbranch_vccz .Lfc1_eexp
	v_max_f32_e32 v80, v226, v226
	v_max_f32_e32 v82, 0, v80
	s_and_saveexec_b64 s[0:1], s[6:7]
	v_exp_f32_e64 v80, -v82
	s_nop 0
	ds_write_b32 v223, v80 offset:49152
	s_or_b64 exec, exec, s[0:1]
	v_add_u32_e32 v210, s78, v224
	s_waitcnt lgkmcnt(0)
	v_add_u32_e32 v251, 0xc000, v210
	ds_read2_b32 v[228:229], v251 offset1:1
	v_add_u32_e32 v251, 0xc008, v210
	ds_read2_b32 v[230:231], v251 offset1:1
	v_add_u32_e32 v251, 0xc020, v210
	ds_read2_b32 v[244:245], v251 offset1:1
	v_add_u32_e32 v251, 0xc028, v210
	ds_read2_b32 v[246:247], v251 offset1:1
	v_add_u32_e32 v251, 0xc040, v210
	ds_read2_b32 v[248:249], v251 offset1:1
	v_add_u32_e32 v251, 0xc048, v210
	ds_read2_b32 v[206:207], v251 offset1:1
	v_add_u32_e32 v251, 0xc060, v210
	ds_read2_b32 v[252:253], v251 offset1:1
	v_add_u32_e32 v251, 0xc068, v210
	ds_read2_b32 v[202:203], v251 offset1:1
	v_add_f32_e32 v225, v225, v82
	v_xor_b32_e32 v80, 0x80000000, v225
	v_pk_add_f32 v[96:97], v[96:97], v[82:83] op_sel_hi:[1,0] neg_lo:[0,1] neg_hi:[0,1]
	v_pk_add_f32 v[112:113], v[112:113], v[82:83] op_sel_hi:[1,0] neg_lo:[0,1] neg_hi:[0,1]
	v_pk_add_f32 v[98:99], v[98:99], v[82:83] op_sel_hi:[1,0] neg_lo:[0,1] neg_hi:[0,1]
	v_pk_add_f32 v[114:115], v[114:115], v[82:83] op_sel_hi:[1,0] neg_lo:[0,1] neg_hi:[0,1]
	v_pk_add_f32 v[100:101], v[100:101], v[82:83] op_sel_hi:[1,0] neg_lo:[0,1] neg_hi:[0,1]
	v_pk_add_f32 v[116:117], v[116:117], v[82:83] op_sel_hi:[1,0] neg_lo:[0,1] neg_hi:[0,1]
	v_pk_add_f32 v[102:103], v[102:103], v[82:83] op_sel_hi:[1,0] neg_lo:[0,1] neg_hi:[0,1]
	v_pk_add_f32 v[118:119], v[118:119], v[82:83] op_sel_hi:[1,0] neg_lo:[0,1] neg_hi:[0,1]
	v_pk_add_f32 v[104:105], v[104:105], v[82:83] op_sel_hi:[1,0] neg_lo:[0,1] neg_hi:[0,1]
	v_pk_add_f32 v[120:121], v[120:121], v[82:83] op_sel_hi:[1,0] neg_lo:[0,1] neg_hi:[0,1]
	v_pk_add_f32 v[106:107], v[106:107], v[82:83] op_sel_hi:[1,0] neg_lo:[0,1] neg_hi:[0,1]
	v_pk_add_f32 v[122:123], v[122:123], v[82:83] op_sel_hi:[1,0] neg_lo:[0,1] neg_hi:[0,1]
	v_pk_add_f32 v[108:109], v[108:109], v[82:83] op_sel_hi:[1,0] neg_lo:[0,1] neg_hi:[0,1]
	v_pk_add_f32 v[124:125], v[124:125], v[82:83] op_sel_hi:[1,0] neg_lo:[0,1] neg_hi:[0,1]
	v_pk_add_f32 v[110:111], v[110:111], v[82:83] op_sel_hi:[1,0] neg_lo:[0,1] neg_hi:[0,1]
	v_pk_add_f32 v[126:127], v[126:127], v[82:83] op_sel_hi:[1,0] neg_lo:[0,1] neg_hi:[0,1]
	v_mov_b32_e32 v81, v80
	v_mov_b32_e32 v82, v80
	v_mov_b32_e32 v83, v80
	v_mov_b32_e32 v84, v80
	v_mov_b32_e32 v85, v80
	v_mov_b32_e32 v86, v80
	v_mov_b32_e32 v87, v80
	v_mov_b32_e32 v88, v80
	v_mov_b32_e32 v89, v80
	v_mov_b32_e32 v90, v80
	v_mov_b32_e32 v91, v80
	v_mov_b32_e32 v92, v80
	v_mov_b32_e32 v93, v80
	v_mov_b32_e32 v94, v80
	v_mov_b32_e32 v95, v80
	s_waitcnt lgkmcnt(0)
	v_pk_mul_f32 v[64:65], v[64:65], v[228:229]
	v_pk_mul_f32 v[66:67], v[66:67], v[230:231]
	v_pk_mul_f32 v[68:69], v[68:69], v[244:245]
	v_pk_mul_f32 v[70:71], v[70:71], v[246:247]
	v_pk_mul_f32 v[72:73], v[72:73], v[248:249]
	v_pk_mul_f32 v[74:75], v[74:75], v[206:207]
	v_pk_mul_f32 v[76:77], v[76:77], v[252:253]
	v_pk_mul_f32 v[78:79], v[78:79], v[202:203]
	v_pk_mul_f32 v[48:49], v[48:49], v[228:229]
	v_pk_mul_f32 v[50:51], v[50:51], v[230:231]
	v_pk_mul_f32 v[52:53], v[52:53], v[244:245]
	v_pk_mul_f32 v[54:55], v[54:55], v[246:247]
	v_pk_mul_f32 v[56:57], v[56:57], v[248:249]
	v_pk_mul_f32 v[58:59], v[58:59], v[206:207]
	v_pk_mul_f32 v[60:61], v[60:61], v[252:253]
	v_pk_mul_f32 v[62:63], v[62:63], v[202:203]
	v_pk_mul_f32 v[32:33], v[32:33], v[228:229]
	v_pk_mul_f32 v[34:35], v[34:35], v[230:231]
	v_pk_mul_f32 v[36:37], v[36:37], v[244:245]
	v_pk_mul_f32 v[38:39], v[38:39], v[246:247]
	v_pk_mul_f32 v[40:41], v[40:41], v[248:249]
	v_pk_mul_f32 v[42:43], v[42:43], v[206:207]
	v_pk_mul_f32 v[44:45], v[44:45], v[252:253]
	v_pk_mul_f32 v[46:47], v[46:47], v[202:203]
	v_pk_mul_f32 v[16:17], v[16:17], v[228:229]
	v_pk_mul_f32 v[18:19], v[18:19], v[230:231]
	v_pk_mul_f32 v[20:21], v[20:21], v[244:245]
	v_pk_mul_f32 v[22:23], v[22:23], v[246:247]
	v_pk_mul_f32 v[24:25], v[24:25], v[248:249]
	v_pk_mul_f32 v[26:27], v[26:27], v[206:207]
	v_pk_mul_f32 v[28:29], v[28:29], v[252:253]
	v_pk_mul_f32 v[30:31], v[30:31], v[202:203]
	v_pk_mul_f32 v[0:1], v[0:1], v[228:229]
	v_pk_mul_f32 v[2:3], v[2:3], v[230:231]
	v_pk_mul_f32 v[4:5], v[4:5], v[244:245]
	v_pk_mul_f32 v[6:7], v[6:7], v[246:247]
	v_pk_mul_f32 v[8:9], v[8:9], v[248:249]
	v_pk_mul_f32 v[10:11], v[10:11], v[206:207]
	v_pk_mul_f32 v[12:13], v[12:13], v[252:253]
	v_pk_mul_f32 v[14:15], v[14:15], v[202:203]
.Lfc1_eexp:
	v_exp_f32_e32 v96, v96
	v_exp_f32_e32 v112, v112
	v_exp_f32_e32 v97, v97
	v_exp_f32_e32 v113, v113
	v_exp_f32_e32 v100, v100
	v_exp_f32_e32 v116, v116
	v_exp_f32_e32 v101, v101
	v_exp_f32_e32 v117, v117
	v_exp_f32_e32 v104, v104
	v_exp_f32_e32 v120, v120
	v_exp_f32_e32 v105, v105
	v_exp_f32_e32 v121, v121
	v_exp_f32_e32 v108, v108
	v_exp_f32_e32 v124, v124
	v_exp_f32_e32 v109, v109
	v_exp_f32_e32 v125, v125
	v_exp_f32_e32 v98, v98
	v_exp_f32_e32 v114, v114
	v_exp_f32_e32 v99, v99
	v_exp_f32_e32 v115, v115
	v_exp_f32_e32 v102, v102
	v_exp_f32_e32 v118, v118
	v_exp_f32_e32 v103, v103
	v_exp_f32_e32 v119, v119
	v_exp_f32_e32 v106, v106
	v_exp_f32_e32 v122, v122
	v_exp_f32_e32 v107, v107
	v_exp_f32_e32 v123, v123
	v_exp_f32_e32 v110, v110
	v_exp_f32_e32 v126, v126
	v_exp_f32_e32 v111, v111
	v_exp_f32_e32 v127, v127
	v_cvt_pk_fp8_f32 v160, v96, v97
	v_cvt_pk_fp8_f32 v164, v112, v113
	v_cvt_pk_fp8_f32 v161, v100, v101
	v_cvt_pk_fp8_f32 v165, v116, v117
	v_cvt_pk_fp8_f32 v162, v104, v105
	v_cvt_pk_fp8_f32 v166, v120, v121
	v_cvt_pk_fp8_f32 v163, v108, v109
	v_cvt_pk_fp8_f32 v167, v124, v125
	v_cvt_pk_fp8_f32 v160, v98, v99 op_sel:[0,0,1]
	v_cvt_pk_fp8_f32 v164, v114, v115 op_sel:[0,0,1]
	v_cvt_pk_fp8_f32 v161, v102, v103 op_sel:[0,0,1]
	v_cvt_pk_fp8_f32 v165, v118, v119 op_sel:[0,0,1]
	v_cvt_pk_fp8_f32 v162, v106, v107 op_sel:[0,0,1]
	v_cvt_pk_fp8_f32 v166, v122, v123 op_sel:[0,0,1]
	v_cvt_pk_fp8_f32 v163, v110, v111 op_sel:[0,0,1]
	v_cvt_pk_fp8_f32 v167, v126, v127 op_sel:[0,0,1]
	s_lshl_b32 s0, s12, 12
	s_add_i32 s0, s91, s0
	s_lshl_b32 s1, s13, 13
	s_add_i32 s1, s91, s1
	v_add_u32_e32 v232, s0, v222
	v_add_u32_e32 v233, s0, v221
	v_add_u32_e32 v234, s1, v222
	v_add_u32_e32 v235, s1, v221
	s_add_i32 s10, s12, 3
	s_and_b32 s10, s10, 3
	s_add_i32 s33, s10, 3
	s_and_b32 s33, s33, 3
	s_lshl_b32 s33, s33, 13
	s_add_i32 s33, s33, s79
	s_addk_i32 s33, 0x4000
	s_add_i32 s32, s86, s2
	s_add_i32 s50, s32, -1
	s_mov_b32 s51, 0
	s_lshl_b64 s[50:51], s[50:51], 6
	s_add_u32 s50, s97, s50
	s_addc_u32 s51, s87, s51
	s_mov_b32 m0, s33
	s_nop 0
	global_load_lds_dwordx4 v218, s[50:51]
	ds_read_b128 v[144:147], v232
	ds_read_b128 v[148:151], v233
	ds_read_b128 v[152:155], v232 offset:2048
	ds_read_b128 v[156:159], v233 offset:2048
	ds_read_b128 v[176:179], v234 offset:16384
	ds_read_b128 v[180:183], v235 offset:16384
	ds_read_b128 v[168:171], v234 offset:18432
	ds_read_b128 v[172:175], v235 offset:18432
	ds_read_b128 v[192:195], v234 offset:20480
	ds_read_b128 v[196:199], v235 offset:20480
	ds_read_b128 v[184:187], v234 offset:22528
	ds_read_b128 v[188:191], v235 offset:22528
	s_add_i32 s0, s12, 1
	s_and_b32 s0, s0, 3
	s_lshl_b32 s0, s0, 12
	s_add_i32 s0, s91, s0
	s_lshl_b32 s1, s12, 13
	s_add_i32 s1, s91, s1
	v_add_u32_e32 v232, s0, v222
	v_add_u32_e32 v233, s0, v221
	v_add_u32_e32 v234, s1, v222
	v_add_u32_e32 v235, s1, v221
	s_add_i32 s10, s12, 4
	s_and_b32 s10, s10, 3
	s_add_i32 s33, s10, 3
	s_and_b32 s33, s33, 3
	s_lshl_b32 s33, s33, 13
	s_add_i32 s33, s33, s79
	s_addk_i32 s33, 0x4000
	s_add_i32 s32, s86, s2
	s_add_i32 s32, s32, 1
	s_add_i32 s50, s32, -1
	s_mov_b32 s51, 0
	s_lshl_b64 s[50:51], s[50:51], 6
	s_add_u32 s50, s97, s50
	s_addc_u32 s51, s87, s51
	s_waitcnt vmcnt(2)
	s_waitcnt lgkmcnt(0)
	s_barrier
	s_mov_b32 s13, s12
	s_add_i32 s12, s12, 1
	s_and_b32 s12, s12, 3
	s_add_i32 s2, s2, 1
	s_add_i32 s3, s3, 64
	s_cmp_lt_u32 s2, s16
	s_cbranch_scc0 .Lfc1_drainA
.Lfc1_even:
	v_mfma_scale_f32_32x32x64_f8f6f4 v[96:111], v[144:151], v[128:135], v[80:95], v220, v220 op_sel_hi:[0,0,0]
	s_mov_b32 m0, s33
	s_nop 0
	global_load_lds_dwordx4 v218, s[50:51]
	s_add_i32 s10, s12, 4
	s_and_b32 s10, s10, 3
	s_add_i32 s33, s10, 3
	s_and_b32 s33, s33, 3
	s_lshl_b32 s33, s33, 13
	s_add_i32 s33, s33, s79
	s_addk_i32 s33, 0x4000
	v_mfma_scale_f32_32x32x64_f8f6f4 v[112:127], v[152:159], v[128:135], v[80:95], v220, v220 op_sel_hi:[0,0,0]
	s_add_i32 s32, s86, s2
	s_add_i32 s32, s32, 1
	s_add_i32 s50, s32, -1
	s_mov_b32 s51, 0
	s_lshl_b64 s[50:51], s[50:51], 6
	s_add_u32 s50, s97, s50
	s_addc_u32 s51, s87, s51
	v_mfma_scale_f32_32x32x64_f8f6f4 v[0:15], v[160:167], v[136:143], v[0:15], v219, v219 op_sel_hi:[0,0,0]
	ds_read_b128 v[144:147], v232
	ds_read_b128 v[148:151], v233
	ds_read_b128 v[152:155], v232 offset:2048
	ds_read_b128 v[156:159], v233 offset:2048
	v_max3_f32 v226, v96, v97, v98
	v_max3_f32 v202, v99, v100, v101
	v_max3_f32 v203, v102, v103, v104
	v_max3_f32 v211, v105, v106, v107
	v_max3_f32 v226, v226, v108, v109
	v_max3_f32 v202, v202, v110, v111
	v_max3_f32 v226, v226, v203, v211
	v_max_f32_e32 v226, v226, v202
	v_mfma_scale_f32_32x32x64_f8f6f4 v[64:79], v[160:167], v[176:183], v[64:79], v219, v219 op_sel_hi:[0,0,0]
	v_max3_f32 v227, v112, v113, v114
	v_max3_f32 v202, v115, v116, v117
	v_max3_f32 v203, v118, v119, v120
	v_max3_f32 v211, v121, v122, v123
	v_max3_f32 v227, v227, v124, v125
	v_max3_f32 v202, v202, v126, v127
	v_max3_f32 v227, v227, v203, v211
	v_max_f32_e32 v227, v227, v202
	v_max_f32_e32 v226, v226, v227
	v_mov_b32_e32 v227, v226
	s_nop 1
	v_permlane32_swap_b32_e32 v226, v227
	v_max3_f32 v226, v226, v227, v227
	s_nop 0
	v_cmp_lt_f32_e32 vcc, 0x41000000, v226
	s_cbranch_vccnz .Lfc1e_rare
	v_mfma_scale_f32_32x32x64_f8f6f4 v[48:63], v[160:167], v[168:175], v[48:63], v219, v219 op_sel_hi:[0,0,0]
	ds_read_b128 v[176:179], v234 offset:16384
	ds_read_b128 v[180:183], v235 offset:16384
	v_exp_f32_e32 v96, v96
	v_exp_f32_e32 v112, v112
	v_exp_f32_e32 v97, v97
	v_exp_f32_e32 v113, v113
	v_exp_f32_e32 v100, v100
	v_exp_f32_e32 v116, v116
	v_exp_f32_e32 v101, v101
	v_exp_f32_e32 v117, v117
	v_mfma_scale_f32_32x32x64_f8f6f4 v[32:47], v[160:167], v[192:199], v[32:47], v219, v219 op_sel_hi:[0,0,0]
	ds_read_b128 v[168:171], v234 offset:18432
	ds_read_b128 v[172:175], v235 offset:18432
	v_exp_f32_e32 v104, v104
	v_exp_f32_e32 v120, v120
	v_exp_f32_e32 v105, v105
	v_exp_f32_e32 v121, v121
	v_exp_f32_e32 v108, v108
	v_exp_f32_e32 v124, v124
	v_exp_f32_e32 v109, v109
	v_exp_f32_e32 v125, v125
	v_mfma_scale_f32_32x32x64_f8f6f4 v[16:31], v[160:167], v[184:191], v[16:31], v219, v219 op_sel_hi:[0,0,0]
	ds_read_b128 v[192:195], v234 offset:20480
	ds_read_b128 v[196:199], v235 offset:20480
	v_exp_f32_e32 v98, v98
	v_exp_f32_e32 v114, v114
	v_exp_f32_e32 v99, v99
	v_exp_f32_e32 v115, v115
	v_exp_f32_e32 v102, v102
	v_exp_f32_e32 v118, v118
	v_exp_f32_e32 v103, v103
	v_exp_f32_e32 v119, v119
	ds_read_b128 v[184:187], v234 offset:22528
	ds_read_b128 v[188:191], v235 offset:22528
.Lfc1e_join:
	v_exp_f32_e32 v106, v106
	v_exp_f32_e32 v122, v122
	v_exp_f32_e32 v107, v107
	v_exp_f32_e32 v123, v123
	v_exp_f32_e32 v110, v110
	v_exp_f32_e32 v126, v126
	v_exp_f32_e32 v111, v111
	v_exp_f32_e32 v127, v127
	s_add_i32 s0, s12, 1
	s_and_b32 s0, s0, 3
	s_lshl_b32 s0, s0, 12
	s_add_i32 s0, s91, s0
	s_lshl_b32 s1, s12, 13
	s_add_i32 s1, s91, s1
	v_add_u32_e32 v232, s0, v222
	v_add_u32_e32 v233, s0, v221
	v_add_u32_e32 v234, s1, v222
	v_add_u32_e32 v235, s1, v221
	v_cvt_pk_fp8_f32 v236, v96, v97
	v_cvt_pk_fp8_f32 v240, v112, v113
	v_cvt_pk_fp8_f32 v237, v100, v101
	v_cvt_pk_fp8_f32 v241, v116, v117
	v_cvt_pk_fp8_f32 v238, v104, v105
	v_cvt_pk_fp8_f32 v242, v120, v121
	v_cvt_pk_fp8_f32 v239, v108, v109
	v_cvt_pk_fp8_f32 v243, v124, v125
	v_cvt_pk_fp8_f32 v236, v98, v99 op_sel:[0,0,1]
	v_cvt_pk_fp8_f32 v240, v114, v115 op_sel:[0,0,1]
	v_cvt_pk_fp8_f32 v237, v102, v103 op_sel:[0,0,1]
	v_cvt_pk_fp8_f32 v241, v118, v119 op_sel:[0,0,1]
	v_cvt_pk_fp8_f32 v238, v106, v107 op_sel:[0,0,1]
	v_cvt_pk_fp8_f32 v242, v122, v123 op_sel:[0,0,1]
	v_cvt_pk_fp8_f32 v239, v110, v111 op_sel:[0,0,1]
	v_cvt_pk_fp8_f32 v243, v126, v127 op_sel:[0,0,1]
	s_waitcnt vmcnt(2)
	s_waitcnt lgkmcnt(0)
	s_barrier
	s_mov_b32 s13, s12
	s_add_i32 s12, s12, 1
	s_and_b32 s12, s12, 3
	s_add_i32 s2, s2, 1
	s_add_i32 s3, s3, 64
	s_cmp_lt_u32 s2, s16
	s_cbranch_scc1 .Lfc1_odd
	s_branch .Lfc1_drainB
.Lfc1_odd:
	v_mfma_scale_f32_32x32x64_f8f6f4 v[96:111], v[144:151], v[128:135], v[80:95], v220, v220 op_sel_hi:[0,0,0]
	s_mov_b32 m0, s33
	s_nop 0
	global_load_lds_dwordx4 v218, s[50:51]
	s_add_i32 s10, s12, 4
	s_and_b32 s10, s10, 3
	s_add_i32 s33, s10, 3
	s_and_b32 s33, s33, 3
	s_lshl_b32 s33, s33, 13
	s_add_i32 s33, s33, s79
	s_addk_i32 s33, 0x4000
	v_mfma_scale_f32_32x32x64_f8f6f4 v[112:127], v[152:159], v[128:135], v[80:95], v220, v220 op_sel_hi:[0,0,0]
	s_add_i32 s32, s86, s2
	s_add_i32 s32, s32, 1
	s_add_i32 s50, s32, -1
	s_mov_b32 s51, 0
	s_lshl_b64 s[50:51], s[50:51], 6
	s_add_u32 s50, s97, s50
	s_addc_u32 s51, s87, s51
	v_mfma_scale_f32_32x32x64_f8f6f4 v[0:15], v[236:243], v[136:143], v[0:15], v219, v219 op_sel_hi:[0,0,0]
	ds_read_b128 v[144:147], v232
	ds_read_b128 v[148:151], v233
	ds_read_b128 v[152:155], v232 offset:2048
	ds_read_b128 v[156:159], v233 offset:2048
	v_max3_f32 v226, v96, v97, v98
	v_max3_f32 v202, v99, v100, v101
	v_max3_f32 v203, v102, v103, v104
	v_max3_f32 v211, v105, v106, v107
	v_max3_f32 v226, v226, v108, v109
	v_max3_f32 v202, v202, v110, v111
	v_max3_f32 v226, v226, v203, v211
	v_max_f32_e32 v226, v226, v202
	v_mfma_scale_f32_32x32x64_f8f6f4 v[64:79], v[236:243], v[176:183], v[64:79], v219, v219 op_sel_hi:[0,0,0]
	v_max3_f32 v227, v112, v113, v114
	v_max3_f32 v202, v115, v116, v117
	v_max3_f32 v203, v118, v119, v120
	v_max3_f32 v211, v121, v122, v123
	v_max3_f32 v227, v227, v124, v125
	v_max3_f32 v202, v202, v126, v127
	v_max3_f32 v227, v227, v203, v211
	v_max_f32_e32 v227, v227, v202
	v_max_f32_e32 v226, v226, v227
	v_mov_b32_e32 v227, v226
	s_nop 1
	v_permlane32_swap_b32_e32 v226, v227
	v_max3_f32 v226, v226, v227, v227
	s_nop 0
	v_cmp_lt_f32_e32 vcc, 0x41000000, v226
	s_cbranch_vccnz .Lfc1o_rare
	v_mfma_scale_f32_32x32x64_f8f6f4 v[48:63], v[236:243], v[168:175], v[48:63], v219, v219 op_sel_hi:[0,0,0]
	ds_read_b128 v[176:179], v234 offset:16384
	ds_read_b128 v[180:183], v235 offset:16384
	v_exp_f32_e32 v96, v96
	v_exp_f32_e32 v112, v112
	v_exp_f32_e32 v97, v97
	v_exp_f32_e32 v113, v113
	v_exp_f32_e32 v100, v100
	v_exp_f32_e32 v116, v116
	v_exp_f32_e32 v101, v101
	v_exp_f32_e32 v117, v117
	v_mfma_scale_f32_32x32x64_f8f6f4 v[32:47], v[236:243], v[192:199], v[32:47], v219, v219 op_sel_hi:[0,0,0]
	ds_read_b128 v[168:171], v234 offset:18432
	ds_read_b128 v[172:175], v235 offset:18432
	v_exp_f32_e32 v104, v104
	v_exp_f32_e32 v120, v120
	v_exp_f32_e32 v105, v105
	v_exp_f32_e32 v121, v121
	v_exp_f32_e32 v108, v108
	v_exp_f32_e32 v124, v124
	v_exp_f32_e32 v109, v109
	v_exp_f32_e32 v125, v125
	v_mfma_scale_f32_32x32x64_f8f6f4 v[16:31], v[236:243], v[184:191], v[16:31], v219, v219 op_sel_hi:[0,0,0]
	ds_read_b128 v[192:195], v234 offset:20480
	ds_read_b128 v[196:199], v235 offset:20480
	v_exp_f32_e32 v98, v98
	v_exp_f32_e32 v114, v114
	v_exp_f32_e32 v99, v99
	v_exp_f32_e32 v115, v115
	v_exp_f32_e32 v102, v102
	v_exp_f32_e32 v118, v118
	v_exp_f32_e32 v103, v103
	v_exp_f32_e32 v119, v119
	ds_read_b128 v[184:187], v234 offset:22528
	ds_read_b128 v[188:191], v235 offset:22528
.Lfc1o_join:
	v_exp_f32_e32 v106, v106
	v_exp_f32_e32 v122, v122
	v_exp_f32_e32 v107, v107
	v_exp_f32_e32 v123, v123
	v_exp_f32_e32 v110, v110
	v_exp_f32_e32 v126, v126
	v_exp_f32_e32 v111, v111
	v_exp_f32_e32 v127, v127
	s_add_i32 s0, s12, 1
	s_and_b32 s0, s0, 3
	s_lshl_b32 s0, s0, 12
	s_add_i32 s0, s91, s0
	s_lshl_b32 s1, s12, 13
	s_add_i32 s1, s91, s1
	v_add_u32_e32 v232, s0, v222
	v_add_u32_e32 v233, s0, v221
	v_add_u32_e32 v234, s1, v222
	v_add_u32_e32 v235, s1, v221
	v_cvt_pk_fp8_f32 v160, v96, v97
	v_cvt_pk_fp8_f32 v164, v112, v113
	v_cvt_pk_fp8_f32 v161, v100, v101
	v_cvt_pk_fp8_f32 v165, v116, v117
	v_cvt_pk_fp8_f32 v162, v104, v105
	v_cvt_pk_fp8_f32 v166, v120, v121
	v_cvt_pk_fp8_f32 v163, v108, v109
	v_cvt_pk_fp8_f32 v167, v124, v125
	v_cvt_pk_fp8_f32 v160, v98, v99 op_sel:[0,0,1]
	v_cvt_pk_fp8_f32 v164, v114, v115 op_sel:[0,0,1]
	v_cvt_pk_fp8_f32 v161, v102, v103 op_sel:[0,0,1]
	v_cvt_pk_fp8_f32 v165, v118, v119 op_sel:[0,0,1]
	v_cvt_pk_fp8_f32 v162, v106, v107 op_sel:[0,0,1]
	v_cvt_pk_fp8_f32 v166, v122, v123 op_sel:[0,0,1]
	v_cvt_pk_fp8_f32 v163, v110, v111 op_sel:[0,0,1]
	v_cvt_pk_fp8_f32 v167, v126, v127 op_sel:[0,0,1]
	s_waitcnt vmcnt(2)
	s_waitcnt lgkmcnt(0)
	s_barrier
	s_mov_b32 s13, s12
	s_add_i32 s12, s12, 1
	s_and_b32 s12, s12, 3
	s_add_i32 s2, s2, 1
	s_add_i32 s3, s3, 64
	s_cmp_lt_u32 s2, s16
	s_cbranch_scc1 .Lfc1_even
	s_branch .Lfc1_drainA
